# stack: 3 items in up-GEMM tail, mixer-C refill DMA inside MFMA stream, relaxed first-iteration waits in W_in
# baseline (speedup 1.0000x reference)
.LBB0_337:
	s_add_i32 s42, s19, s18
	s_mov_b32 m0, s42
	v_readfirstlane_b32 s6, v192
	v_readfirstlane_b32 s7, v193
	ds_read_b128 v[204:207], v203 offset:16384
	ds_read_b128 v[208:211], v203 offset:17408
	ds_read_b128 v[222:225], v203 offset:18432
	ds_read_b128 v[226:229], v203 offset:19456
	ds_read_b128 v[244:247], v203 offset:20480
	ds_read_b128 v[248:251], v203 offset:21504
	ds_read_b128 v[180:183], v203 offset:22528
	ds_read_b128 v[184:187], v203 offset:23552
	global_load_lds_dwordx4 v166, s[6:7]
	s_add_i32 m0, s42, 0x2000
	s_add_i32 s42, s20, s18
	global_load_lds_dwordx4 v170, s[6:7]
	s_mov_b32 m0, s42
	v_readfirstlane_b32 s6, v196
	v_readfirstlane_b32 s7, v197
	v_lshl_add_u64 v[198:199], v[200:201], 0, v[218:219]
	v_lshl_add_u64 v[200:201], v[200:201], 0, v[168:169]
	v_mov_b32_e32 v167, v219
	v_mov_b32_e32 v171, v219
	v_lshl_add_u64 v[190:191], v[192:193], 0, v[166:167]
	global_load_lds_dwordx4 v166, s[6:7]
	s_add_i32 m0, s42, 0x2000
	v_lshl_add_u64 v[192:193], v[192:193], 0, v[170:171]
	global_load_lds_dwordx4 v170, s[6:7]
	s_mov_b32 m0, s26
	v_lshl_add_u64 v[194:195], v[196:197], 0, v[166:167]
	global_load_lds_dwordx4 v[198:199], off
	s_add_i32 m0, s26, 0x2000
	v_lshl_add_u64 v[196:197], v[196:197], 0, v[170:171]
	global_load_lds_dwordx4 v[200:201], off
	s_cmp_lg_u32 s14, 0
	s_cbranch_scc1 .Lrwin_n1
	s_cmp_lt_u32 s33, 2
	s_cbranch_scc1 .Lrwin_n1
	s_waitcnt vmcnt(30)
	s_branch .Lrwin_d1
.Lrwin_n1:
	s_waitcnt vmcnt(8)
.Lrwin_d1:
	s_waitcnt lgkmcnt(0)
	s_barrier
	s_setprio 1
	s_waitcnt lgkmcnt(0)
	v_mfma_scale_f32_16x16x128_f8f6f4 v[94:97], v[18:25], v[204:211], v[94:97], v232, v232 op_sel_hi:[0,0,0]
	v_mfma_scale_f32_16x16x128_f8f6f4 v[90:93], v[26:33], v[204:211], v[90:93], v232, v232 op_sel_hi:[0,0,0]
	v_mfma_scale_f32_16x16x128_f8f6f4 v[78:81], v[18:25], v[222:229], v[78:81], v232, v232 op_sel_hi:[0,0,0]
	v_mfma_scale_f32_16x16x128_f8f6f4 v[74:77], v[26:33], v[222:229], v[74:77], v232, v232 op_sel_hi:[0,0,0]
	v_mfma_scale_f32_16x16x128_f8f6f4 v[62:65], v[18:25], v[244:251], v[62:65], v232, v232 op_sel_hi:[0,0,0]
	v_mfma_scale_f32_16x16x128_f8f6f4 v[58:61], v[26:33], v[244:251], v[58:61], v232, v232 op_sel_hi:[0,0,0]
	v_mfma_scale_f32_16x16x128_f8f6f4 v[46:49], v[18:25], v[180:187], v[46:49], v232, v232 op_sel_hi:[0,0,0]
	v_mfma_scale_f32_16x16x128_f8f6f4 v[42:45], v[26:33], v[180:187], v[42:45], v232, v232 op_sel_hi:[0,0,0]
	s_setprio 0
	s_setprio 1
	v_mfma_scale_f32_16x16x128_f8f6f4 v[86:89], v[2:9], v[204:211], v[86:89], v232, v232 op_sel_hi:[0,0,0]
	v_mfma_scale_f32_16x16x128_f8f6f4 v[82:85], v[10:17], v[204:211], v[82:85], v232, v232 op_sel_hi:[0,0,0]
	v_mfma_scale_f32_16x16x128_f8f6f4 v[70:73], v[2:9], v[222:229], v[70:73], v232, v232 op_sel_hi:[0,0,0]
	v_mfma_scale_f32_16x16x128_f8f6f4 v[66:69], v[10:17], v[222:229], v[66:69], v232, v232 op_sel_hi:[0,0,0]
	v_mfma_scale_f32_16x16x128_f8f6f4 v[54:57], v[2:9], v[244:251], v[54:57], v232, v232 op_sel_hi:[0,0,0]
	v_mfma_scale_f32_16x16x128_f8f6f4 v[50:53], v[10:17], v[244:251], v[50:53], v232, v232 op_sel_hi:[0,0,0]
	v_mfma_scale_f32_16x16x128_f8f6f4 v[38:41], v[2:9], v[180:187], v[38:41], v232, v232 op_sel_hi:[0,0,0]
	v_mfma_scale_f32_16x16x128_f8f6f4 v[34:37], v[10:17], v[180:187], v[34:37], v232, v232 op_sel_hi:[0,0,0]
	s_setprio 0
	s_barrier
	v_add_u32_e32 v14, s23, v202
	v_add_u32_e32 v30, s29, v202
	ds_read_b128 v[2:5], v14
	ds_read_b128 v[6:9], v14 offset:1024
	ds_read_b128 v[10:13], v14 offset:2048
	ds_read_b128 v[14:17], v14 offset:3072
	ds_read_b128 v[18:21], v30
	ds_read_b128 v[22:25], v30 offset:1024
	ds_read_b128 v[26:29], v30 offset:2048
	ds_read_b128 v[30:33], v30 offset:3072
	v_lshl_add_u64 v[240:241], v[188:189], 0, v[218:219]
	s_add_i32 m0, s26, 0x4000
	ds_read_b128 v[180:183], v203 offset:32768
	ds_read_b128 v[184:187], v203 offset:33792
	ds_read_b128 v[204:207], v203 offset:34816
	ds_read_b128 v[208:211], v203 offset:35840
	ds_read_b128 v[222:225], v203 offset:36864
	ds_read_b128 v[226:229], v203 offset:37888
	ds_read_b128 v[244:247], v203 offset:38912
	ds_read_b128 v[248:251], v203 offset:39936
	global_load_lds_dwordx4 v[240:241], off
	v_lshl_add_u64 v[188:189], v[188:189], 0, v[168:169]
	s_add_i32 m0, s26, 0x6000
	s_nop 0
	global_load_lds_dwordx4 v[188:189], off
	s_cmp_lg_u32 s14, 0
	s_cbranch_scc1 .Lrwin_n2
	s_cmp_lt_u32 s33, 2
	s_cbranch_scc1 .Lrwin_n2
	s_waitcnt vmcnt(26)
	s_branch .Lrwin_d2

.Lrwin_d2:
	s_waitcnt lgkmcnt(0)
	s_barrier
	s_setprio 1
	s_waitcnt lgkmcnt(0)
	v_mfma_scale_f32_16x16x128_f8f6f4 v[158:161], v[2:9], v[180:187], v[158:161], v232, v232 op_sel_hi:[0,0,0]
	v_mfma_scale_f32_16x16x128_f8f6f4 v[154:157], v[10:17], v[180:187], v[154:157], v232, v232 op_sel_hi:[0,0,0]
	v_mfma_scale_f32_16x16x128_f8f6f4 v[142:145], v[2:9], v[204:211], v[142:145], v232, v232 op_sel_hi:[0,0,0]
	v_mfma_scale_f32_16x16x128_f8f6f4 v[138:141], v[10:17], v[204:211], v[138:141], v232, v232 op_sel_hi:[0,0,0]
	v_mfma_scale_f32_16x16x128_f8f6f4 v[126:129], v[2:9], v[222:229], v[126:129], v232, v232 op_sel_hi:[0,0,0]
	v_mfma_scale_f32_16x16x128_f8f6f4 v[122:125], v[10:17], v[222:229], v[122:125], v232, v232 op_sel_hi:[0,0,0]
	v_mfma_scale_f32_16x16x128_f8f6f4 v[110:113], v[2:9], v[244:251], v[110:113], v232, v232 op_sel_hi:[0,0,0]
	v_mfma_scale_f32_16x16x128_f8f6f4 v[106:109], v[10:17], v[244:251], v[106:109], v232, v232 op_sel_hi:[0,0,0]
	s_setprio 0
	s_setprio 1
	v_mfma_scale_f32_16x16x128_f8f6f4 v[150:153], v[18:25], v[180:187], v[150:153], v232, v232 op_sel_hi:[0,0,0]
	v_mfma_scale_f32_16x16x128_f8f6f4 v[146:149], v[26:33], v[180:187], v[146:149], v232, v232 op_sel_hi:[0,0,0]
	v_mfma_scale_f32_16x16x128_f8f6f4 v[134:137], v[18:25], v[204:211], v[134:137], v232, v232 op_sel_hi:[0,0,0]
	v_mfma_scale_f32_16x16x128_f8f6f4 v[130:133], v[26:33], v[204:211], v[130:133], v232, v232 op_sel_hi:[0,0,0]
	v_mfma_scale_f32_16x16x128_f8f6f4 v[118:121], v[18:25], v[222:229], v[118:121], v232, v232 op_sel_hi:[0,0,0]
	v_mfma_scale_f32_16x16x128_f8f6f4 v[114:117], v[26:33], v[222:229], v[114:117], v232, v232 op_sel_hi:[0,0,0]
	v_mfma_scale_f32_16x16x128_f8f6f4 v[102:105], v[18:25], v[244:251], v[102:105], v232, v232 op_sel_hi:[0,0,0]
	v_mfma_scale_f32_16x16x128_f8f6f4 v[98:101], v[26:33], v[244:251], v[98:101], v232, v232 op_sel_hi:[0,0,0]
	s_setprio 0
	s_barrier
	s_mov_b32 m0, s24
	v_lshl_add_u64 v[188:189], v[190:191], 0, s[72:73]
	ds_read_b128 v[180:183], v203 offset:49152
	ds_read_b128 v[184:187], v203 offset:50176
	ds_read_b128 v[204:207], v203 offset:51200
	ds_read_b128 v[208:211], v203 offset:52224
	ds_read_b128 v[222:225], v203 offset:53248
	ds_read_b128 v[226:229], v203 offset:54272
	ds_read_b128 v[244:247], v203 offset:55296
	ds_read_b128 v[248:251], v203 offset:56320
	global_load_lds_dwordx4 v[188:189], off
	v_lshl_add_u64 v[188:189], v[192:193], 0, s[72:73]
	s_mov_b32 m0, s25
	s_nop 0
	global_load_lds_dwordx4 v[188:189], off
	v_lshl_add_u64 v[188:189], v[194:195], 0, s[72:73]
	s_mov_b32 m0, s30
	s_nop 0
	global_load_lds_dwordx4 v[188:189], off
	v_lshl_add_u64 v[188:189], v[196:197], 0, s[72:73]
	s_mov_b32 m0, s31
	s_nop 0
	global_load_lds_dwordx4 v[188:189], off
	v_lshl_add_u64 v[188:189], v[198:199], 0, s[72:73]
	s_mov_b32 m0, s27
	s_nop 0
	global_load_lds_dwordx4 v[188:189], off
	v_lshl_add_u64 v[188:189], v[200:201], 0, s[72:73]
	s_mov_b32 m0, s28
	s_nop 0
	global_load_lds_dwordx4 v[188:189], off
	s_waitcnt vmcnt(8)
	s_waitcnt lgkmcnt(0)
	s_barrier
	s_setprio 1
	s_waitcnt lgkmcnt(0)
	v_mfma_scale_f32_16x16x128_f8f6f4 v[94:97], v[2:9], v[180:187], v[94:97], v232, v232 op_sel_hi:[0,0,0]
	v_mfma_scale_f32_16x16x128_f8f6f4 v[90:93], v[10:17], v[180:187], v[90:93], v232, v232 op_sel_hi:[0,0,0]
	v_mfma_scale_f32_16x16x128_f8f6f4 v[78:81], v[2:9], v[204:211], v[78:81], v232, v232 op_sel_hi:[0,0,0]
	v_mfma_scale_f32_16x16x128_f8f6f4 v[74:77], v[10:17], v[204:211], v[74:77], v232, v232 op_sel_hi:[0,0,0]
	v_mfma_scale_f32_16x16x128_f8f6f4 v[62:65], v[2:9], v[222:229], v[62:65], v232, v232 op_sel_hi:[0,0,0]
	v_mfma_scale_f32_16x16x128_f8f6f4 v[58:61], v[10:17], v[222:229], v[58:61], v232, v232 op_sel_hi:[0,0,0]
	v_mfma_scale_f32_16x16x128_f8f6f4 v[46:49], v[2:9], v[244:251], v[46:49], v232, v232 op_sel_hi:[0,0,0]
	v_mfma_scale_f32_16x16x128_f8f6f4 v[42:45], v[10:17], v[244:251], v[42:45], v232, v232 op_sel_hi:[0,0,0]
	s_setprio 0
	s_setprio 1
	v_mfma_scale_f32_16x16x128_f8f6f4 v[86:89], v[18:25], v[180:187], v[86:89], v232, v232 op_sel_hi:[0,0,0]
	v_mfma_scale_f32_16x16x128_f8f6f4 v[82:85], v[26:33], v[180:187], v[82:85], v232, v232 op_sel_hi:[0,0,0]
	v_mfma_scale_f32_16x16x128_f8f6f4 v[70:73], v[18:25], v[204:211], v[70:73], v232, v232 op_sel_hi:[0,0,0]
	v_mfma_scale_f32_16x16x128_f8f6f4 v[66:69], v[26:33], v[204:211], v[66:69], v232, v232 op_sel_hi:[0,0,0]
	v_mfma_scale_f32_16x16x128_f8f6f4 v[54:57], v[18:25], v[222:229], v[54:57], v232, v232 op_sel_hi:[0,0,0]
	v_mfma_scale_f32_16x16x128_f8f6f4 v[50:53], v[26:33], v[222:229], v[50:53], v232, v232 op_sel_hi:[0,0,0]
	v_mfma_scale_f32_16x16x128_f8f6f4 v[38:41], v[18:25], v[244:251], v[38:41], v232, v232 op_sel_hi:[0,0,0]
	v_mfma_scale_f32_16x16x128_f8f6f4 v[34:37], v[26:33], v[244:251], v[34:37], v232, v232 op_sel_hi:[0,0,0]
	s_setprio 0
	s_barrier
	s_add_i32 s41, s41, 2
	s_add_u32 s14, s14, 0x100
	s_addc_u32 s15, s15, 0
	s_cmp_gt_u32 s41, 5
	s_cbranch_scc1 .LBB0_345
.LBB0_338:
	v_add_u32_e32 v2, s19, v202
	v_add_u32_e32 v14, s20, v202
	ds_read_b128 v[18:21], v2
	ds_read_b128 v[22:25], v2 offset:1024
	ds_read_b128 v[26:29], v2 offset:2048
	ds_read_b128 v[30:33], v2 offset:3072
	ds_read_b128 v[2:5], v14
	ds_read_b128 v[6:9], v14 offset:1024
	ds_read_b128 v[10:13], v14 offset:2048
	ds_read_b128 v[14:17], v14 offset:3072
	v_lshl_add_u64 v[188:189], v[176:177], 0, s[14:15]
	v_lshl_add_u64 v[180:181], v[188:189], 0, v[218:219]
	v_lshl_add_u64 v[180:181], v[180:181], 0, s[74:75]
	s_add_i32 m0, s26, 0xc000
	v_mov_b32_e32 v169, v219
	ds_read_b128 v[190:193], v203
	ds_read_b128 v[194:197], v203 offset:1024
	ds_read_b128 v[204:207], v203 offset:2048
	ds_read_b128 v[208:211], v203 offset:3072
	ds_read_b128 v[244:247], v203 offset:4096
	ds_read_b128 v[248:251], v203 offset:5120
	ds_read_b128 v[222:225], v203 offset:6144
	ds_read_b128 v[226:229], v203 offset:7168
	global_load_lds_dwordx4 v[180:181], off
	v_lshl_add_u64 v[180:181], v[188:189], 0, v[168:169]
	v_lshl_add_u64 v[180:181], v[180:181], 0, s[74:75]
	s_add_i32 m0, s26, 0xe000
	s_nop 0
	global_load_lds_dwordx4 v[180:181], off
	s_cmp_lg_u32 s14, 0
	s_cbranch_scc1 .Lrwin_n0
	s_cmp_lt_u32 s33, 2
	s_cbranch_scc1 .Lrwin_n0
	s_waitcnt vmcnt(26)
	s_branch .Lrwin_d0

.Lrwin_d0:
	s_waitcnt lgkmcnt(0)
	s_barrier
	s_setprio 1
	s_waitcnt lgkmcnt(0)
	v_mfma_scale_f32_16x16x128_f8f6f4 v[158:161], v[18:25], v[190:197], v[158:161], v232, v232 op_sel_hi:[0,0,0]
	v_mfma_scale_f32_16x16x128_f8f6f4 v[154:157], v[26:33], v[190:197], v[154:157], v232, v232 op_sel_hi:[0,0,0]
	v_mfma_scale_f32_16x16x128_f8f6f4 v[142:145], v[18:25], v[204:211], v[142:145], v232, v232 op_sel_hi:[0,0,0]
	v_mfma_scale_f32_16x16x128_f8f6f4 v[138:141], v[26:33], v[204:211], v[138:141], v232, v232 op_sel_hi:[0,0,0]
	v_mfma_scale_f32_16x16x128_f8f6f4 v[126:129], v[18:25], v[244:251], v[126:129], v232, v232 op_sel_hi:[0,0,0]
	v_mfma_scale_f32_16x16x128_f8f6f4 v[122:125], v[26:33], v[244:251], v[122:125], v232, v232 op_sel_hi:[0,0,0]
	v_mfma_scale_f32_16x16x128_f8f6f4 v[110:113], v[18:25], v[222:229], v[110:113], v232, v232 op_sel_hi:[0,0,0]
	v_mfma_scale_f32_16x16x128_f8f6f4 v[106:109], v[26:33], v[222:229], v[106:109], v232, v232 op_sel_hi:[0,0,0]
	s_setprio 0
	s_setprio 1
	v_mfma_scale_f32_16x16x128_f8f6f4 v[150:153], v[2:9], v[190:197], v[150:153], v232, v232 op_sel_hi:[0,0,0]
	v_mfma_scale_f32_16x16x128_f8f6f4 v[146:149], v[10:17], v[190:197], v[146:149], v232, v232 op_sel_hi:[0,0,0]
	v_mfma_scale_f32_16x16x128_f8f6f4 v[134:137], v[2:9], v[204:211], v[134:137], v232, v232 op_sel_hi:[0,0,0]
	v_mfma_scale_f32_16x16x128_f8f6f4 v[130:133], v[10:17], v[204:211], v[130:133], v232, v232 op_sel_hi:[0,0,0]
	v_mfma_scale_f32_16x16x128_f8f6f4 v[118:121], v[2:9], v[244:251], v[118:121], v232, v232 op_sel_hi:[0,0,0]
	v_mfma_scale_f32_16x16x128_f8f6f4 v[114:117], v[10:17], v[244:251], v[114:117], v232, v232 op_sel_hi:[0,0,0]
	v_mfma_scale_f32_16x16x128_f8f6f4 v[102:105], v[2:9], v[222:229], v[102:105], v232, v232 op_sel_hi:[0,0,0]
	v_mfma_scale_f32_16x16x128_f8f6f4 v[98:101], v[10:17], v[222:229], v[98:101], v232, v232 op_sel_hi:[0,0,0]
	s_cmpk_lg_i32 s14, 0x300
	s_setprio 0
	s_barrier
	s_cbranch_scc0 .LBB0_340
	s_mov_b64 s[6:7], 0x20100
	v_lshl_add_u64 v[200:201], v[188:189], 0, s[76:77]
	v_lshl_add_u64 v[180:181], v[178:179], 0, s[14:15]
	v_lshl_add_u64 v[188:189], v[188:189], 0, s[6:7]
	s_mov_b64 s[6:7], 0x8100
	v_lshl_add_u64 v[192:193], v[180:181], 0, s[76:77]
	v_lshl_add_u64 v[196:197], v[180:181], 0, s[6:7]
	s_cbranch_execnz .LBB0_337
	s_branch .LBB0_341
